# sleepdiag
# baseline (speedup 1.0000x reference)
.LBB0_4:
	s_or_b64 exec, exec, s[2:3]
	v_mov_b32_e32 v1, 0
	s_waitcnt lgkmcnt(0)
	s_barrier
	ds_read2_b32 v[32:33], v1 offset0:3 offset1:7
	ds_read2_b32 v[34:35], v1 offset0:1 offset1:2
	ds_read2_b32 v[36:37], v1 offset0:5 offset1:6
	s_movk_i32 s6, 0xc0
	v_cmp_gt_u32_e32 vcc, s6, v0
	s_movk_i32 s6, 0x80
	s_waitcnt lgkmcnt(2)
	v_fmac_f32_e32 v33, 0, v32
	v_cndmask_b32_e32 v1, 0, v33, vcc
	s_waitcnt lgkmcnt(0)
	v_fma_f32 v32, v35, v1, v37
	v_cmp_gt_u32_e32 vcc, s6, v0
	s_load_dwordx4 s[0:3], s[0:1], 0x30
	s_nop 0
	v_cndmask_b32_e32 v1, v1, v32, vcc
	v_fmac_f32_e32 v36, v34, v1
	v_cmp_gt_u32_e32 vcc, 64, v0
	s_nop 1
	v_cndmask_b32_e32 v0, v1, v36, vcc
	v_mov_b32_e32 v1, s5
	v_fmac_f32_e32 v1, s4, v0
	v_fmac_f32_e32 v24, v28, v1
	v_fmac_f32_e32 v30, v31, v0
	s_nop 0
	v_mov_b32_dpp v1, v24 wave_shl:1 row_mask:0xf bank_mask:0xf
	v_fmac_f32_e32 v13, v23, v1
	v_mov_b32_dpp v0, v30 wave_shl:1 row_mask:0xf bank_mask:0xf
	v_fmac_f32_e32 v12, v22, v13
	v_fmac_f32_e32 v17, v29, v0
	v_fmac_f32_e32 v11, v21, v12
	v_fmac_f32_e32 v16, v27, v17
	v_fmac_f32_e32 v10, v20, v11
	s_waitcnt lgkmcnt(0)
	v_lshl_add_u64 v[20:21], s[0:1], 0, v[18:19]
	v_fmac_f32_e32 v15, v26, v16
	v_pk_add_f32 v[4:5], v[12:13], v[4:5]
	v_pk_add_f32 v[2:3], v[10:11], v[2:3]
	s_sleep 16
	global_store_dwordx4 v[20:21], v[10:13], off nt
	v_fmac_f32_e32 v14, v25, v15
	v_pk_add_f32 v[0:1], v[14:15], v[6:7]
	v_lshl_add_u64 v[10:11], s[2:3], 0, v[18:19]
	global_store_dwordx4 v[10:11], v[2:5], off nt
	s_nop 1
	v_pk_add_f32 v[2:3], v[16:17], v[8:9]
	global_store_dwordx4 v[20:21], v[14:17], off offset:1024 nt
	global_store_dwordx4 v[10:11], v[0:3], off offset:1024 nt
	s_endpgm
